# speedup vs baseline: 1.0498x; 1.0024x over previous
_Z22k2_resolve_rank_gatherPKfS0_PKdS0_PKiPKyPKtS0_S4_Pf:
	s_load_dwordx16 s[4:19], s[0:1], 0x0
	s_load_dwordx4 s[20:23], s[0:1], 0x40
	s_and_b32 s3, s2, 7
	s_lshr_b32 s2, s2, 3
	s_lshl_b32 s3, s3, 7
	s_add_u32 s2, s2, s3
	v_and_b32_e32 v1, 0x3ff, v0
	s_lshr_b32 s24, s2, 6
	s_and_b32 s25, s2, 63
	s_lshl_b32 s26, s24, 9
	v_lshl_add_u32 v2, v1, 1, s26
	v_lshlrev_b32_e32 v3, 4, v2
	v_lshlrev_b32_e32 v24, 2, v2
	v_lshlrev_b32_e32 v25, 3, v2
	v_mov_b32_e32 v106, 0
	v_mov_b32_e32 v107, 0
	v_mov_b32_e32 v105, 0x1800
	v_lshlrev_b32_e32 v104, 3, v1
	s_movk_i32 s30, 0x641
	s_mov_b32 s32, 0xa0b5ed8d
	s_mov_b32 s33, 0x3ed0c6f7
	s_mov_b32 s34, 0xa0b5ed8d
	s_mov_b32 s35, 0xbed0c6f7
	s_mul_i32 s31, s26, 0x1904
	v_lshrrev_b32_e32 v29, 6, v1
	s_waitcnt lgkmcnt(0)
	global_load_dwordx4 v[4:7], v3, s[16:17]
	global_load_dwordx4 v[8:11], v3, s[16:17] offset:16
	global_load_dwordx2 v[12:13], v24, s[10:11]
	global_load_dwordx2 v[16:17], v24, s[12:13]
	global_load_dwordx4 v[20:23], v25, s[8:9]
	global_load_dwordx2 v[14:15], v24, s[18:19]
	global_load_dwordx2 v[18:19], v24, s[20:21]
	s_add_u32 s28, s4, s31
	s_addc_u32 s29, s5, 0
	v_readfirstlane_b32 s27, v29
	ds_write_b64 v105, v[106:107]
	ds_write_b64 v105, v[106:107] offset:8
	ds_write_b64 v105, v[106:107] offset:16
	ds_write_b64 v104, v[106:107] offset:8448
	s_mov_b64 s[36:37], 0
	s_mov_b64 s[38:39], 0
	s_mov_b64 s[40:41], 0
	s_mov_b64 s[42:43], 0
	s_mov_b64 s[44:45], 0
	v_lshlrev_b32_e32 v2, 4, v1
	s_waitcnt vmcnt(2)
	ds_write_b128 v2, v[20:23] offset:12544
	v_lshlrev_b32_e32 v3, 5, v1
	ds_write_b128 v3, v[4:7] offset:22784
	ds_write_b128 v3, v[8:11] offset:22800
	ds_write_b64 v104, v[16:17] offset:30976
	v_and_b32_e32 v26, 0xffff, v4
	v_and_b32_e32 v27, 0xffff, v8
	v_max_u32_e32 v28, v26, v27
	v_cvt_f64_f32_e32 v[92:93], v12
	v_cvt_f64_f32_e32 v[94:95], v13
	v_add_f64 v[92:93], v[92:93], -v[20:21]
	v_add_f64 v[94:95], v[94:95], -v[22:23]
	s_waitcnt vmcnt(0)
	ds_write_b64 v104, v[14:15] offset:33024
	v_cvt_f64_f32_e32 v[96:97], v14
	v_cvt_f64_f32_e32 v[98:99], v15
	v_add_f64 v[96:97], v[96:97], -v[20:21]
	v_add_f64 v[98:99], v[98:99], -v[22:23]
	s_waitcnt lgkmcnt(0)
	s_barrier
	v_cmp_lt_u32_e32 vcc, 0, v28
	s_cbranch_vccz .Lk2_l1_done
	v_cmp_lt_u32_e32 vcc, 0, v26
	s_and_saveexec_b64 s[46:47], vcc
	s_cbranch_execz .Lk2_l1_0_0
	v_lshrrev_b32_e32 v29, 16, v4
	v_mad_u32_u24 v30, v29, s30, v16
	v_lshlrev_b32_e32 v30, 2, v30
	v_lshlrev_b32_e32 v29, 3, v29
	global_load_dword v32, v30, s[28:29]
	ds_read_b64 v[34:35], v29 offset:12544
.Lk2_l1_0_0:
	s_or_b64 exec, exec, s[46:47]
	v_cmp_lt_u32_e32 vcc, 0, v27
	s_and_saveexec_b64 s[46:47], vcc
	s_cbranch_execz .Lk2_l1_0_1
	v_lshrrev_b32_e32 v29, 16, v8
	v_mad_u32_u24 v30, v29, s30, v17
	v_lshlrev_b32_e32 v30, 2, v30
	v_lshlrev_b32_e32 v29, 3, v29
	global_load_dword v36, v30, s[28:29]
	ds_read_b64 v[38:39], v29 offset:12544
.Lk2_l1_0_1:
	s_or_b64 exec, exec, s[46:47]
	v_cmp_lt_u32_e32 vcc, 1, v28
	s_cbranch_vccz .Lk2_l1_done
	v_cmp_lt_u32_e32 vcc, 1, v26
	s_and_saveexec_b64 s[46:47], vcc
	s_cbranch_execz .Lk2_l1_1_0
	v_and_b32_e32 v29, 0xffff, v5
	v_mad_u32_u24 v30, v29, s30, v16
	v_lshlrev_b32_e32 v30, 2, v30
	v_lshlrev_b32_e32 v29, 3, v29
	global_load_dword v40, v30, s[28:29]
	ds_read_b64 v[42:43], v29 offset:12544
.Lk2_l1_1_0:
	s_or_b64 exec, exec, s[46:47]
	v_cmp_lt_u32_e32 vcc, 1, v27
	s_and_saveexec_b64 s[46:47], vcc
	s_cbranch_execz .Lk2_l1_1_1
	v_and_b32_e32 v29, 0xffff, v9
	v_mad_u32_u24 v30, v29, s30, v17
	v_lshlrev_b32_e32 v30, 2, v30
	v_lshlrev_b32_e32 v29, 3, v29
	global_load_dword v44, v30, s[28:29]
	ds_read_b64 v[46:47], v29 offset:12544
.Lk2_l1_1_1:
	s_or_b64 exec, exec, s[46:47]
	v_cmp_lt_u32_e32 vcc, 2, v28
	s_cbranch_vccz .Lk2_l1_done
	v_cmp_lt_u32_e32 vcc, 2, v26
	s_and_saveexec_b64 s[46:47], vcc
	s_cbranch_execz .Lk2_l1_2_0
	v_lshrrev_b32_e32 v29, 16, v5
	v_mad_u32_u24 v30, v29, s30, v16
	v_lshlrev_b32_e32 v30, 2, v30
	v_lshlrev_b32_e32 v29, 3, v29
	global_load_dword v48, v30, s[28:29]
	ds_read_b64 v[50:51], v29 offset:12544
.Lk2_l1_2_0:
	s_or_b64 exec, exec, s[46:47]
	v_cmp_lt_u32_e32 vcc, 2, v27
	s_and_saveexec_b64 s[46:47], vcc
	s_cbranch_execz .Lk2_l1_2_1
	v_lshrrev_b32_e32 v29, 16, v9
	v_mad_u32_u24 v30, v29, s30, v17
	v_lshlrev_b32_e32 v30, 2, v30
	v_lshlrev_b32_e32 v29, 3, v29
	global_load_dword v52, v30, s[28:29]
	ds_read_b64 v[54:55], v29 offset:12544
.Lk2_l1_2_1:
	s_or_b64 exec, exec, s[46:47]
	v_cmp_lt_u32_e32 vcc, 3, v28
	s_cbranch_vccz .Lk2_l1_done
	v_cmp_lt_u32_e32 vcc, 3, v26
	s_and_saveexec_b64 s[46:47], vcc
	s_cbranch_execz .Lk2_l1_3_0
	v_and_b32_e32 v29, 0xffff, v6
	v_mad_u32_u24 v30, v29, s30, v16
	v_lshlrev_b32_e32 v30, 2, v30
	v_lshlrev_b32_e32 v29, 3, v29
	global_load_dword v56, v30, s[28:29]
	ds_read_b64 v[58:59], v29 offset:12544
.Lk2_l1_3_0:
	s_or_b64 exec, exec, s[46:47]
	v_cmp_lt_u32_e32 vcc, 3, v27
	s_and_saveexec_b64 s[46:47], vcc
	s_cbranch_execz .Lk2_l1_3_1
	v_and_b32_e32 v29, 0xffff, v10
	v_mad_u32_u24 v30, v29, s30, v17
	v_lshlrev_b32_e32 v30, 2, v30
	v_lshlrev_b32_e32 v29, 3, v29
	global_load_dword v60, v30, s[28:29]
	ds_read_b64 v[62:63], v29 offset:12544
.Lk2_l1_3_1:
	s_or_b64 exec, exec, s[46:47]
	v_cmp_lt_u32_e32 vcc, 4, v28
	s_cbranch_vccz .Lk2_l1_done
	v_cmp_lt_u32_e32 vcc, 4, v26
	s_and_saveexec_b64 s[46:47], vcc
	s_cbranch_execz .Lk2_l1_4_0
	v_lshrrev_b32_e32 v29, 16, v6
	v_mad_u32_u24 v30, v29, s30, v16
	v_lshlrev_b32_e32 v30, 2, v30
	v_lshlrev_b32_e32 v29, 3, v29
	global_load_dword v64, v30, s[28:29]
	ds_read_b64 v[66:67], v29 offset:12544
.Lk2_l1_4_0:
	s_or_b64 exec, exec, s[46:47]
	v_cmp_lt_u32_e32 vcc, 4, v27
	s_and_saveexec_b64 s[46:47], vcc
	s_cbranch_execz .Lk2_l1_4_1
	v_lshrrev_b32_e32 v29, 16, v10
	v_mad_u32_u24 v30, v29, s30, v17
	v_lshlrev_b32_e32 v30, 2, v30
	v_lshlrev_b32_e32 v29, 3, v29
	global_load_dword v68, v30, s[28:29]
	ds_read_b64 v[70:71], v29 offset:12544
.Lk2_l1_4_1:
	s_or_b64 exec, exec, s[46:47]
	v_cmp_lt_u32_e32 vcc, 5, v28
	s_cbranch_vccz .Lk2_l1_done
	v_cmp_lt_u32_e32 vcc, 5, v26
	s_and_saveexec_b64 s[46:47], vcc
	s_cbranch_execz .Lk2_l1_5_0
	v_and_b32_e32 v29, 0xffff, v7
	v_mad_u32_u24 v30, v29, s30, v16
	v_lshlrev_b32_e32 v30, 2, v30
	v_lshlrev_b32_e32 v29, 3, v29
	global_load_dword v72, v30, s[28:29]
	ds_read_b64 v[74:75], v29 offset:12544
.Lk2_l1_5_0:
	s_or_b64 exec, exec, s[46:47]
	v_cmp_lt_u32_e32 vcc, 5, v27
	s_and_saveexec_b64 s[46:47], vcc
	s_cbranch_execz .Lk2_l1_5_1
	v_and_b32_e32 v29, 0xffff, v11
	v_mad_u32_u24 v30, v29, s30, v17
	v_lshlrev_b32_e32 v30, 2, v30
	v_lshlrev_b32_e32 v29, 3, v29
	global_load_dword v76, v30, s[28:29]
	ds_read_b64 v[78:79], v29 offset:12544
.Lk2_l1_5_1:
	s_or_b64 exec, exec, s[46:47]
	v_cmp_lt_u32_e32 vcc, 6, v28
	s_cbranch_vccz .Lk2_l1_done
	v_cmp_lt_u32_e32 vcc, 6, v26
	s_and_saveexec_b64 s[46:47], vcc
	s_cbranch_execz .Lk2_l1_6_0
	v_lshrrev_b32_e32 v29, 16, v7
	v_mad_u32_u24 v30, v29, s30, v16
	v_lshlrev_b32_e32 v30, 2, v30
	v_lshlrev_b32_e32 v29, 3, v29
	global_load_dword v80, v30, s[28:29]
	ds_read_b64 v[82:83], v29 offset:12544
.Lk2_l1_6_0:
	s_or_b64 exec, exec, s[46:47]
	v_cmp_lt_u32_e32 vcc, 6, v27
	s_and_saveexec_b64 s[46:47], vcc
	s_cbranch_execz .Lk2_l1_6_1
	v_lshrrev_b32_e32 v29, 16, v11
	v_mad_u32_u24 v30, v29, s30, v17
	v_lshlrev_b32_e32 v30, 2, v30
	v_lshlrev_b32_e32 v29, 3, v29
	global_load_dword v84, v30, s[28:29]
	ds_read_b64 v[86:87], v29 offset:12544

.Lk2_l1_done:
	s_waitcnt vmcnt(0) lgkmcnt(0)
	v_cmp_lt_u32_e32 vcc, 0, v28
	s_cbranch_vccz .Lk2_l2_done
	v_cmp_lt_u32_e32 vcc, 0, v26
	s_and_saveexec_b64 s[46:47], vcc
	s_cbranch_execz .Lk2_l2_0_0
	v_cvt_f64_f32_e32 v[88:89], v32
	v_add_f64 v[88:89], v[88:89], -v[34:35]
	v_add_f64 v[88:89], v[88:89], -v[92:93]
	v_cmp_le_f64_e32 vcc, s[34:35], v[88:89]
	v_cmp_ge_f64_e64 s[48:49], s[32:33], v[88:89]
	s_or_b64 s[36:37], s[36:37], vcc
	s_and_b64 s[48:49], s[48:49], vcc
	s_or_b64 s[44:45], s[44:45], s[48:49]
.Lk2_l2_0_0:
	s_or_b64 exec, exec, s[46:47]
	v_cmp_lt_u32_e32 vcc, 0, v27
	s_and_saveexec_b64 s[46:47], vcc
	s_cbranch_execz .Lk2_l2_0_1
	v_cvt_f64_f32_e32 v[88:89], v36
	v_add_f64 v[88:89], v[88:89], -v[38:39]
	v_add_f64 v[88:89], v[88:89], -v[94:95]
	v_cmp_le_f64_e32 vcc, s[34:35], v[88:89]
	v_cmp_ge_f64_e64 s[48:49], s[32:33], v[88:89]
	s_or_b64 s[40:41], s[40:41], vcc
	s_and_b64 s[48:49], s[48:49], vcc
	s_or_b64 s[44:45], s[44:45], s[48:49]
.Lk2_l2_0_1:
	s_or_b64 exec, exec, s[46:47]
	v_cmp_lt_u32_e32 vcc, 1, v28
	s_cbranch_vccz .Lk2_l2_done
	v_cmp_lt_u32_e32 vcc, 1, v26
	s_and_saveexec_b64 s[46:47], vcc
	s_cbranch_execz .Lk2_l2_1_0
	v_cvt_f64_f32_e32 v[88:89], v40
	v_add_f64 v[88:89], v[88:89], -v[42:43]
	v_add_f64 v[88:89], v[88:89], -v[92:93]
	v_cmp_le_f64_e32 vcc, s[34:35], v[88:89]
	v_cmp_ge_f64_e64 s[48:49], s[32:33], v[88:89]
	s_or_b64 s[36:37], s[36:37], vcc
	s_and_b64 s[48:49], s[48:49], vcc
	s_or_b64 s[44:45], s[44:45], s[48:49]
.Lk2_l2_1_0:
	s_or_b64 exec, exec, s[46:47]
	v_cmp_lt_u32_e32 vcc, 1, v27
	s_and_saveexec_b64 s[46:47], vcc
	s_cbranch_execz .Lk2_l2_1_1
	v_cvt_f64_f32_e32 v[88:89], v44
	v_add_f64 v[88:89], v[88:89], -v[46:47]
	v_add_f64 v[88:89], v[88:89], -v[94:95]
	v_cmp_le_f64_e32 vcc, s[34:35], v[88:89]
	v_cmp_ge_f64_e64 s[48:49], s[32:33], v[88:89]
	s_or_b64 s[40:41], s[40:41], vcc
	s_and_b64 s[48:49], s[48:49], vcc
	s_or_b64 s[44:45], s[44:45], s[48:49]
.Lk2_l2_1_1:
	s_or_b64 exec, exec, s[46:47]
	v_cmp_lt_u32_e32 vcc, 2, v28
	s_cbranch_vccz .Lk2_l2_done
	v_cmp_lt_u32_e32 vcc, 2, v26
	s_and_saveexec_b64 s[46:47], vcc
	s_cbranch_execz .Lk2_l2_2_0
	v_cvt_f64_f32_e32 v[88:89], v48
	v_add_f64 v[88:89], v[88:89], -v[50:51]
	v_add_f64 v[88:89], v[88:89], -v[92:93]
	v_cmp_le_f64_e32 vcc, s[34:35], v[88:89]
	v_cmp_ge_f64_e64 s[48:49], s[32:33], v[88:89]
	s_or_b64 s[36:37], s[36:37], vcc
	s_and_b64 s[48:49], s[48:49], vcc
	s_or_b64 s[44:45], s[44:45], s[48:49]
.Lk2_l2_2_0:
	s_or_b64 exec, exec, s[46:47]
	v_cmp_lt_u32_e32 vcc, 2, v27
	s_and_saveexec_b64 s[46:47], vcc
	s_cbranch_execz .Lk2_l2_2_1
	v_cvt_f64_f32_e32 v[88:89], v52
	v_add_f64 v[88:89], v[88:89], -v[54:55]
	v_add_f64 v[88:89], v[88:89], -v[94:95]
	v_cmp_le_f64_e32 vcc, s[34:35], v[88:89]
	v_cmp_ge_f64_e64 s[48:49], s[32:33], v[88:89]
	s_or_b64 s[40:41], s[40:41], vcc
	s_and_b64 s[48:49], s[48:49], vcc
	s_or_b64 s[44:45], s[44:45], s[48:49]
.Lk2_l2_2_1:
	s_or_b64 exec, exec, s[46:47]
	v_cmp_lt_u32_e32 vcc, 3, v28
	s_cbranch_vccz .Lk2_l2_done
	v_cmp_lt_u32_e32 vcc, 3, v26
	s_and_saveexec_b64 s[46:47], vcc
	s_cbranch_execz .Lk2_l2_3_0
	v_cvt_f64_f32_e32 v[88:89], v56
	v_add_f64 v[88:89], v[88:89], -v[58:59]
	v_add_f64 v[88:89], v[88:89], -v[92:93]
	v_cmp_le_f64_e32 vcc, s[34:35], v[88:89]
	v_cmp_ge_f64_e64 s[48:49], s[32:33], v[88:89]
	s_or_b64 s[36:37], s[36:37], vcc
	s_and_b64 s[48:49], s[48:49], vcc
	s_or_b64 s[44:45], s[44:45], s[48:49]
.Lk2_l2_3_0:
	s_or_b64 exec, exec, s[46:47]
	v_cmp_lt_u32_e32 vcc, 3, v27
	s_and_saveexec_b64 s[46:47], vcc
	s_cbranch_execz .Lk2_l2_3_1
	v_cvt_f64_f32_e32 v[88:89], v60
	v_add_f64 v[88:89], v[88:89], -v[62:63]
	v_add_f64 v[88:89], v[88:89], -v[94:95]
	v_cmp_le_f64_e32 vcc, s[34:35], v[88:89]
	v_cmp_ge_f64_e64 s[48:49], s[32:33], v[88:89]
	s_or_b64 s[40:41], s[40:41], vcc
	s_and_b64 s[48:49], s[48:49], vcc
	s_or_b64 s[44:45], s[44:45], s[48:49]
.Lk2_l2_3_1:
	s_or_b64 exec, exec, s[46:47]
	v_cmp_lt_u32_e32 vcc, 4, v28
	s_cbranch_vccz .Lk2_l2_done
	v_cmp_lt_u32_e32 vcc, 4, v26
	s_and_saveexec_b64 s[46:47], vcc
	s_cbranch_execz .Lk2_l2_4_0
	v_cvt_f64_f32_e32 v[88:89], v64
	v_add_f64 v[88:89], v[88:89], -v[66:67]
	v_add_f64 v[88:89], v[88:89], -v[92:93]
	v_cmp_le_f64_e32 vcc, s[34:35], v[88:89]
	v_cmp_ge_f64_e64 s[48:49], s[32:33], v[88:89]
	s_or_b64 s[36:37], s[36:37], vcc
	s_and_b64 s[48:49], s[48:49], vcc
	s_or_b64 s[44:45], s[44:45], s[48:49]
.Lk2_l2_4_0:
	s_or_b64 exec, exec, s[46:47]
	v_cmp_lt_u32_e32 vcc, 4, v27
	s_and_saveexec_b64 s[46:47], vcc
	s_cbranch_execz .Lk2_l2_4_1
	v_cvt_f64_f32_e32 v[88:89], v68
	v_add_f64 v[88:89], v[88:89], -v[70:71]
	v_add_f64 v[88:89], v[88:89], -v[94:95]
	v_cmp_le_f64_e32 vcc, s[34:35], v[88:89]
	v_cmp_ge_f64_e64 s[48:49], s[32:33], v[88:89]
	s_or_b64 s[40:41], s[40:41], vcc
	s_and_b64 s[48:49], s[48:49], vcc
	s_or_b64 s[44:45], s[44:45], s[48:49]
.Lk2_l2_4_1:
	s_or_b64 exec, exec, s[46:47]
	v_cmp_lt_u32_e32 vcc, 5, v28
	s_cbranch_vccz .Lk2_l2_done
	v_cmp_lt_u32_e32 vcc, 5, v26
	s_and_saveexec_b64 s[46:47], vcc
	s_cbranch_execz .Lk2_l2_5_0
	v_cvt_f64_f32_e32 v[88:89], v72
	v_add_f64 v[88:89], v[88:89], -v[74:75]
	v_add_f64 v[88:89], v[88:89], -v[92:93]
	v_cmp_le_f64_e32 vcc, s[34:35], v[88:89]
	v_cmp_ge_f64_e64 s[48:49], s[32:33], v[88:89]
	s_or_b64 s[36:37], s[36:37], vcc
	s_and_b64 s[48:49], s[48:49], vcc
	s_or_b64 s[44:45], s[44:45], s[48:49]
.Lk2_l2_5_0:
	s_or_b64 exec, exec, s[46:47]
	v_cmp_lt_u32_e32 vcc, 5, v27
	s_and_saveexec_b64 s[46:47], vcc
	s_cbranch_execz .Lk2_l2_5_1
	v_cvt_f64_f32_e32 v[88:89], v76
	v_add_f64 v[88:89], v[88:89], -v[78:79]
	v_add_f64 v[88:89], v[88:89], -v[94:95]
	v_cmp_le_f64_e32 vcc, s[34:35], v[88:89]
	v_cmp_ge_f64_e64 s[48:49], s[32:33], v[88:89]
	s_or_b64 s[40:41], s[40:41], vcc
	s_and_b64 s[48:49], s[48:49], vcc
	s_or_b64 s[44:45], s[44:45], s[48:49]
.Lk2_l2_5_1:
	s_or_b64 exec, exec, s[46:47]
	v_cmp_lt_u32_e32 vcc, 6, v28
	s_cbranch_vccz .Lk2_l2_done
	v_cmp_lt_u32_e32 vcc, 6, v26
	s_and_saveexec_b64 s[46:47], vcc
	s_cbranch_execz .Lk2_l2_6_0
	v_cvt_f64_f32_e32 v[88:89], v80
	v_add_f64 v[88:89], v[88:89], -v[82:83]
	v_add_f64 v[88:89], v[88:89], -v[92:93]
	v_cmp_le_f64_e32 vcc, s[34:35], v[88:89]
	v_cmp_ge_f64_e64 s[48:49], s[32:33], v[88:89]
	s_or_b64 s[36:37], s[36:37], vcc
	s_and_b64 s[48:49], s[48:49], vcc
	s_or_b64 s[44:45], s[44:45], s[48:49]
.Lk2_l2_6_0:
	s_or_b64 exec, exec, s[46:47]
	v_cmp_lt_u32_e32 vcc, 6, v27
	s_and_saveexec_b64 s[46:47], vcc
	s_cbranch_execz .Lk2_l2_6_1
	v_cvt_f64_f32_e32 v[88:89], v84
	v_add_f64 v[88:89], v[88:89], -v[86:87]
	v_add_f64 v[88:89], v[88:89], -v[94:95]
	v_cmp_le_f64_e32 vcc, s[34:35], v[88:89]
	v_cmp_ge_f64_e64 s[48:49], s[32:33], v[88:89]
	s_or_b64 s[40:41], s[40:41], vcc
	s_and_b64 s[48:49], s[48:49], vcc
	s_or_b64 s[44:45], s[44:45], s[48:49]

.Lk2_t15_loop0:
	s_cmp_eq_u64 s[50:51], 0
	s_cbranch_scc1 .Lk2_t15_done0
	s_ff1_i32_b64 s56, s[50:51]
	s_bitset0_b64 s[50:51], s56
	s_lshl_b32 s57, s27, 6
	s_add_u32 s57, s57, s56
	s_lshl_b32 s57, s57, 1
	s_lshl_b32 s58, s57, 4
	v_readlane_b32 s59, v16, s56
	v_readlane_b32 s60, v92, s56
	v_readlane_b32 s61, v93, s56
	v_readlane_b32 s70, v18, s56
	v_readlane_b32 s72, v96, s56
	v_readlane_b32 s73, v97, s56
	v_and_b32_e32 v32, 7, v1
	v_bfe_u32 v33, v1, 3, 3
	v_lshlrev_b32_e32 v34, 1, v32
	v_add_u32_e32 v34, s58, v34
	v_mov_b32_e32 v35, s58
	ds_read_u16 v36, v34 offset:22786
	ds_read_u16 v37, v35 offset:22784
	v_mov_b32_e32 v43, s59
	v_mov_b32_e32 v60, s60
	v_mov_b32_e32 v61, s61
	s_waitcnt lgkmcnt(0)
	v_cmp_lt_u32_e64 s[62:63], v32, v37
	s_nop 1
	v_cndmask_b32_e64 v36, 0, v36, s[62:63]
	v_lshlrev_b32_e32 v38, 4, v36
	v_lshl_add_u32 v39, v33, 1, v38
	ds_read_u16 v40, v39 offset:22786
	ds_read_u16 v41, v38 offset:22784
	v_lshlrev_b32_e32 v42, 3, v36
	ds_read_b64 v[44:45], v42 offset:12544
	v_mad_u32_u24 v46, v36, s30, v43
	v_lshlrev_b32_e32 v46, 2, v46
	global_load_dword v47, v46, s[28:29]
	v_mov_b32_e32 v52, s70
	v_mad_u32_u24 v52, v36, s30, v52
	v_lshlrev_b32_e32 v52, 2, v52
	global_load_dword v63, v52, s[28:29]
	s_waitcnt lgkmcnt(0)
	v_cmp_lt_u32_e64 s[64:65], v33, v41
	s_and_b64 s[64:65], s[64:65], s[62:63]
	v_cndmask_b32_e64 v40, 0, v40, s[64:65]
	v_lshlrev_b32_e32 v48, 3, v40
	ds_read_b64 v[50:51], v48 offset:12544
	v_mad_u32_u24 v49, v40, s30, v43
	v_lshlrev_b32_e32 v49, 2, v49
	global_load_dword v62, v49, s[28:29]
	s_waitcnt vmcnt(0) lgkmcnt(0)
	v_cvt_f64_f32_e32 v[52:53], v63
	v_add_f64 v[52:53], v[52:53], -v[44:45]
	v_add_f64 v[52:53], v[52:53], -s[72:73]
	v_cmp_le_f64_e64 s[66:67], s[34:35], v[52:53]
	v_cmp_ge_f64_e64 s[68:69], s[32:33], v[52:53]
	s_and_b64 s[66:67], s[66:67], s[62:63]
	s_and_b32 s66, s66, 0xff
	s_and_b32 s68, s68, s66
	s_cmp_eq_u32 s68, 0
	s_cbranch_scc1 .Lk2_t15_nounc0
	s_or_b32 s44, s44, 1
.Lk2_t15_nounc0:
	s_cmp_eq_u32 s66, 0
	s_cbranch_scc1 .Lk2_t15_c2ok0
	s_bitset1_b64 s[38:39], s56
	s_branch .Lk2_t15_loop0
.Lk2_t15_c2ok0:
	v_cvt_f64_f32_e32 v[54:55], v47
	v_cvt_f64_f32_e32 v[56:57], v62
	v_add_f64 v[54:55], v[54:55], -v[44:45]
	v_add_f64 v[56:57], v[56:57], -v[50:51]
	v_add_f64 v[58:59], v[54:55], -v[60:61]
	v_add_f64 v[56:57], v[56:57], -v[54:55]
	v_cmp_lt_f64_e64 s[66:67], s[32:33], v[58:59]
	v_cmp_le_f64_e64 s[68:69], s[34:35], v[56:57]
	s_and_b64 s[66:67], s[66:67], s[62:63]
	s_and_b32 s66, s66, 0xff
	s_and_b64 s[68:69], s[68:69], s[64:65]
	s_or_b32 s68, s68, s69
	s_lshr_b32 s69, s68, 16
	s_or_b32 s68, s68, s69
	s_lshr_b32 s69, s68, 8
	s_or_b32 s68, s68, s69
	s_andn2_b32 s66, s66, s68
	s_and_b32 s66, s66, 0xff
	s_cmp_eq_u32 s66, 0
	s_cbranch_scc1 .Lk2_t15_loop0
	s_bitset1_b64 s[52:53], s56
	s_bitset0_b64 s[36:37], s56
	s_branch .Lk2_t15_loop0

.Lk2_t15_loop1:
	s_cmp_eq_u64 s[50:51], 0
	s_cbranch_scc1 .Lk2_t15_done1
	s_ff1_i32_b64 s56, s[50:51]
	s_bitset0_b64 s[50:51], s56
	s_lshl_b32 s57, s27, 6
	s_add_u32 s57, s57, s56
	s_lshl_b32 s57, s57, 1
	s_add_u32 s57, s57, 1
	s_lshl_b32 s58, s57, 4
	v_readlane_b32 s59, v17, s56
	v_readlane_b32 s60, v94, s56
	v_readlane_b32 s61, v95, s56
	v_readlane_b32 s70, v19, s56
	v_readlane_b32 s72, v98, s56
	v_readlane_b32 s73, v99, s56
	v_and_b32_e32 v32, 7, v1
	v_bfe_u32 v33, v1, 3, 3
	v_lshlrev_b32_e32 v34, 1, v32
	v_add_u32_e32 v34, s58, v34
	v_mov_b32_e32 v35, s58
	ds_read_u16 v36, v34 offset:22786
	ds_read_u16 v37, v35 offset:22784
	v_mov_b32_e32 v43, s59
	v_mov_b32_e32 v60, s60
	v_mov_b32_e32 v61, s61
	s_waitcnt lgkmcnt(0)
	v_cmp_lt_u32_e64 s[62:63], v32, v37
	s_nop 1
	v_cndmask_b32_e64 v36, 0, v36, s[62:63]
	v_lshlrev_b32_e32 v38, 4, v36
	v_lshl_add_u32 v39, v33, 1, v38
	ds_read_u16 v40, v39 offset:22786
	ds_read_u16 v41, v38 offset:22784
	v_lshlrev_b32_e32 v42, 3, v36
	ds_read_b64 v[44:45], v42 offset:12544
	v_mad_u32_u24 v46, v36, s30, v43
	v_lshlrev_b32_e32 v46, 2, v46
	global_load_dword v47, v46, s[28:29]
	v_mov_b32_e32 v52, s70
	v_mad_u32_u24 v52, v36, s30, v52
	v_lshlrev_b32_e32 v52, 2, v52
	global_load_dword v63, v52, s[28:29]
	s_waitcnt lgkmcnt(0)
	v_cmp_lt_u32_e64 s[64:65], v33, v41
	s_and_b64 s[64:65], s[64:65], s[62:63]
	v_cndmask_b32_e64 v40, 0, v40, s[64:65]
	v_lshlrev_b32_e32 v48, 3, v40
	ds_read_b64 v[50:51], v48 offset:12544
	v_mad_u32_u24 v49, v40, s30, v43
	v_lshlrev_b32_e32 v49, 2, v49
	global_load_dword v62, v49, s[28:29]
	s_waitcnt vmcnt(0) lgkmcnt(0)
	v_cvt_f64_f32_e32 v[52:53], v63
	v_add_f64 v[52:53], v[52:53], -v[44:45]
	v_add_f64 v[52:53], v[52:53], -s[72:73]
	v_cmp_le_f64_e64 s[66:67], s[34:35], v[52:53]
	v_cmp_ge_f64_e64 s[68:69], s[32:33], v[52:53]
	s_and_b64 s[66:67], s[66:67], s[62:63]
	s_and_b32 s66, s66, 0xff
	s_and_b32 s68, s68, s66
	s_cmp_eq_u32 s68, 0
	s_cbranch_scc1 .Lk2_t15_nounc1
	s_or_b32 s44, s44, 1
.Lk2_t15_nounc1:
	s_cmp_eq_u32 s66, 0
	s_cbranch_scc1 .Lk2_t15_c2ok1
	s_bitset1_b64 s[42:43], s56
	s_branch .Lk2_t15_loop1
.Lk2_t15_c2ok1:
	v_cvt_f64_f32_e32 v[54:55], v47
	v_cvt_f64_f32_e32 v[56:57], v62
	v_add_f64 v[54:55], v[54:55], -v[44:45]
	v_add_f64 v[56:57], v[56:57], -v[50:51]
	v_add_f64 v[58:59], v[54:55], -v[60:61]
	v_add_f64 v[56:57], v[56:57], -v[54:55]
	v_cmp_lt_f64_e64 s[66:67], s[32:33], v[58:59]
	v_cmp_le_f64_e64 s[68:69], s[34:35], v[56:57]
	s_and_b64 s[66:67], s[66:67], s[62:63]
	s_and_b32 s66, s66, 0xff
	s_and_b64 s[68:69], s[68:69], s[64:65]
	s_or_b32 s68, s68, s69
	s_lshr_b32 s69, s68, 16
	s_or_b32 s68, s68, s69
	s_lshr_b32 s69, s68, 8
	s_or_b32 s68, s68, s69
	s_andn2_b32 s66, s66, s68
	s_and_b32 s66, s66, 0xff
	s_cmp_eq_u32 s66, 0
	s_cbranch_scc1 .Lk2_t15_loop1
	s_bitset1_b64 s[54:55], s56
	s_bitset0_b64 s[40:41], s56
	s_branch .Lk2_t15_loop1
